# speedup vs baseline: 1.0061x; 1.0031x over previous
.LBB2_6:
	s_or_b64 exec, exec, s[18:19]
	v_xor_b32_e32 v23, 32, v23
	s_add_i32 s38, 0, 0x1c000
	v_lshlrev_b32_e32 v23, 2, v23
	v_lshlrev_b32_e32 v199, 2, v25
	s_waitcnt vmcnt(4) lgkmcnt(0)
	s_barrier
	v_add3_u32 v23, s38, v23, v199
	ds_read_b32 v23, v23
	v_max_f32_e32 v24, v24, v24
	v_mul_f32_e32 v22, 0x3db8aa3b, v22
	v_mov_b32_e32 v164, 0
	v_mov_b32_e32 v165, 0
	s_waitcnt lgkmcnt(0)
	s_movk_i32 s45, 0x4000
	v_add3_u32 v250, s45, v184, v185
	v_add3_u32 v251, s45, v184, v186
	v_add3_u32 v252, s45, v184, v187
	v_add3_u32 v253, s45, v184, v188
	ds_read_b128 v[218:221], v250 offset:49152
	ds_read_b128 v[222:225], v251 offset:49152
	ds_read_b128 v[242:245], v252 offset:49152
	ds_read_b128 v[246:249], v253 offset:49152
	v_add3_u32 v250, s45, v184, v189
	v_add3_u32 v251, s45, v184, v190
	v_add3_u32 v252, s45, v184, v191
	v_add3_u32 v253, s45, v184, v192
	ds_read_b128 v[202:205], v250 offset:49152
	ds_read_b128 v[206:209], v251 offset:49152
	ds_read_b128 v[210:213], v252 offset:49152
	ds_read_b128 v[214:217], v253 offset:49152
	v_max_f32_e32 v23, v23, v23
	v_max_f32_e32 v197, v24, v23
	v_mov_b32_e32 v23, 2.0
	v_fmamk_f32 v200, v197, 0xbdb8aa3b, v23
	v_fmamk_f32 v23, v22, 0xcb400000, v200
	v_fma_f32 v2, v2, v22, v23
	v_fma_f32 v3, v3, v22, v23
	v_fma_f32 v6, v6, v22, v23
	v_fma_f32 v7, v7, v22, v23
	v_fma_f32 v10, v10, v22, v23
	v_fma_f32 v11, v11, v22, v23
	v_fma_f32 v14, v14, v22, v23
	v_fma_f32 v15, v15, v22, v23
	v_exp_f32_e32 v2, v2
	v_exp_f32_e32 v3, v3
	v_exp_f32_e32 v6, v6
	v_exp_f32_e32 v7, v7
	v_exp_f32_e32 v10, v10
	v_exp_f32_e32 v11, v11
	v_exp_f32_e32 v14, v14
	v_exp_f32_e32 v15, v15
	v_fma_f32 v4, v4, v22, v23
	v_fma_f32 v5, v5, v22, v23
	v_fma_f32 v8, v8, v22, v23
	v_fma_f32 v9, v9, v22, v23
	v_fma_f32 v12, v12, v22, v23
	v_fma_f32 v13, v13, v22, v23
	v_fma_f32 v16, v16, v22, v23
	v_fmac_f32_e32 v23, v17, v22
	v_mov_b32_e32 v166, 0
	v_mov_b32_e32 v167, 0
	v_exp_f32_e32 v4, v4
	v_exp_f32_e32 v5, v5
	v_exp_f32_e32 v8, v8
	v_exp_f32_e32 v9, v9
	v_exp_f32_e32 v12, v12
	v_exp_f32_e32 v13, v13
	v_exp_f32_e32 v16, v16
	v_exp_f32_e32 v17, v23
	v_add_f32_e32 v250, v2, v3
	v_add_f32_e32 v251, v4, v5
	v_add_f32_e32 v252, v6, v7
	v_add_f32_e32 v253, v8, v9
	v_add_f32_e32 v250, v250, v251
	v_add_f32_e32 v252, v252, v253
	v_add_f32_e32 v251, v10, v11
	v_add_f32_e32 v253, v12, v13
	v_add_f32_e32 v250, v250, v252
	v_add_f32_e32 v251, v251, v253
	v_add_f32_e32 v252, v14, v15
	v_add_f32_e32 v253, v16, v17
	v_add_f32_e32 v250, v250, v251
	v_add_f32_e32 v252, v252, v253
	v_add_f32_e32 v250, v250, v252
	v_cvt_pk_fp8_f32 v164, v2, v3
	v_cvt_pk_fp8_f32 v165, v6, v7
	v_cvt_pk_fp8_f32 v166, v10, v11
	v_cvt_pk_fp8_f32 v167, v14, v15
	s_lshl_b32 s0, s22, 11
	s_add_i32 s0, s0, 0
	s_add_i32 s0, s0, 0x18000
	v_cvt_pk_fp8_f32 v164, v4, v5 op_sel:[0,0,1]
	v_cvt_pk_fp8_f32 v165, v8, v9 op_sel:[0,0,1]
	v_cvt_pk_fp8_f32 v166, v12, v13 op_sel:[0,0,1]
	v_cvt_pk_fp8_f32 v167, v16, v17 op_sel:[0,0,1]
	v_lshl_add_u32 v193, v198, 4, s0
	v_lshrrev_b32_e32 v3, 2, v0
	v_lshlrev_b32_e32 v6, 1, v183
	s_lshl_b32 s0, s20, 20
	v_bfe_u32 v4, v0, 2, 2
	v_lshl_or_b32 v5, v1, 6, s24
	v_bitop3_b32 v3, v6, v3, 3 bitop3:0x78
	s_or_b32 s18, s0, s23
	v_lshl_add_u32 v194, s34, 10, v193
	v_lshl_or_b32 v195, v3, 4, v5
	v_bitop3_b32 v3, v6, v4, 1 bitop3:0x36
	v_add3_u32 v4, s21, v20, v21
	s_add_u32 s0, s6, s18
	ds_write_b128 v194, v[164:167]
	v_lshl_or_b32 v196, v3, 4, v5
	v_ashrrev_i32_e32 v5, 31, v4
	s_addc_u32 s1, s7, 0
	s_waitcnt vmcnt(2) lgkmcnt(0)
	s_barrier
	s_mov_b64 s[60:61], s[0:1]
	v_lshl_add_u64 v[170:171], s[0:1], 0, v[4:5]
	v_add3_u32 v4, s21, v18, v19
	s_add_u32 s0, s8, s18
	v_mov_b32_e32 v2, 0
	v_ashrrev_i32_e32 v5, 31, v4
	s_addc_u32 s1, s9, 0
	s_mov_b32 s39, 0
	s_mov_b32 s40, 1
	s_mov_b64 s[64:65], s[0:1]
	v_lshl_add_u64 v[172:173], s[0:1], 0, v[4:5]
	s_mov_b64 s[6:7], 0
	s_movk_i32 s41, 0x2000
	s_mov_b64 s[8:9], 0xc000
	s_mov_b64 s[18:19], 0xe000
	s_mov_b64 s[20:21], 0x8000
	s_mov_b64 s[22:23], 0xa000
	s_mov_b32 s42, 0x42966666
	v_mov_b32_e32 v82, 0x4b400000
	v_mov_b32_e32 v100, 0x38383838
	s_mov_b32 s0, 0
	s_mov_b32 s43, 1
	v_mov_b32_e32 v3, v2
	v_mov_b32_e32 v4, v2
	v_mov_b32_e32 v5, v2
	v_mov_b32_e32 v6, v2
	v_mov_b32_e32 v7, v2
	v_mov_b32_e32 v8, v2
	v_mov_b32_e32 v9, v2
	v_mov_b32_e32 v10, v2
	v_mov_b32_e32 v11, v2
	v_mov_b32_e32 v12, v2
	v_mov_b32_e32 v13, v2
	v_mov_b32_e32 v14, v2
	v_mov_b32_e32 v15, v2
	v_mov_b32_e32 v16, v2
	v_mov_b32_e32 v17, v2
	v_mov_b32_e32 v18, v2
	v_mov_b32_e32 v19, v2
	v_mov_b32_e32 v20, v2
	v_mov_b32_e32 v21, v2
	v_mov_b32_e32 v22, v2
	v_mov_b32_e32 v23, v2
	v_mov_b32_e32 v24, v2
	v_mov_b32_e32 v25, v2
	v_mov_b32_e32 v26, v2
	v_mov_b32_e32 v27, v2
	v_mov_b32_e32 v28, v2
	v_mov_b32_e32 v29, v2
	v_mov_b32_e32 v30, v2
	v_mov_b32_e32 v31, v2
	v_mov_b32_e32 v32, v2
	v_mov_b32_e32 v33, v2
	v_mov_b32_e32 v34, v2
	v_mov_b32_e32 v35, v2
	v_mov_b32_e32 v36, v2
	v_mov_b32_e32 v37, v2
	v_mov_b32_e32 v38, v2
	v_mov_b32_e32 v39, v2
	v_mov_b32_e32 v40, v2
	v_mov_b32_e32 v41, v2
	v_mov_b32_e32 v42, v2
	v_mov_b32_e32 v43, v2
	v_mov_b32_e32 v44, v2
	v_mov_b32_e32 v45, v2
	v_mov_b32_e32 v46, v2
	v_mov_b32_e32 v47, v2
	v_mov_b32_e32 v48, v2
	v_mov_b32_e32 v49, v2
	v_mov_b32_e32 v50, v2
	v_mov_b32_e32 v51, v2
	v_mov_b32_e32 v52, v2
	v_mov_b32_e32 v53, v2
	v_mov_b32_e32 v54, v2
	v_mov_b32_e32 v55, v2
	v_mov_b32_e32 v56, v2
	v_mov_b32_e32 v57, v2
	v_mov_b32_e32 v58, v2
	v_mov_b32_e32 v59, v2
	v_mov_b32_e32 v60, v2
	v_mov_b32_e32 v61, v2
	v_mov_b32_e32 v62, v2
	v_mov_b32_e32 v63, v2
	v_mov_b32_e32 v64, v2
	v_mov_b32_e32 v65, v2
	v_mov_b32_e32 v66, v2
	v_mov_b32_e32 v67, v2
	v_mov_b32_e32 v68, v2
	v_mov_b32_e32 v69, v2
	v_mov_b32_e32 v70, v2
	v_mov_b32_e32 v71, v2
	v_mov_b32_e32 v72, v2
	v_mov_b32_e32 v73, v2
	v_mov_b32_e32 v74, v2
	v_mov_b32_e32 v75, v2
	v_mov_b32_e32 v76, v2
	v_mov_b32_e32 v77, v2
	v_mov_b32_e32 v78, v2
	v_mov_b32_e32 v79, v2
	v_mov_b32_e32 v80, v2
	v_mov_b32_e32 v81, v2
	v_mov_b32_e32 v66, v250
	v_mov_b32_e32 v226, 0x4b400000
	v_mov_b32_e32 v227, v226
	v_mov_b32_e32 v228, v226
	v_mov_b32_e32 v229, v226
	v_mov_b32_e32 v230, v226
	v_mov_b32_e32 v231, v226
	v_mov_b32_e32 v232, v226
	v_mov_b32_e32 v233, v226
	v_mov_b32_e32 v234, v226
	v_mov_b32_e32 v235, v226
	v_mov_b32_e32 v236, v226
	v_mov_b32_e32 v237, v226
	v_mov_b32_e32 v238, v226
	v_mov_b32_e32 v239, v226
	v_mov_b32_e32 v240, v226
	v_mov_b32_e32 v241, v226
	v_add_u32_e32 v250, 0xc000, v184
	v_add_u32_e32 v185, v185, v250
	v_add_u32_e32 v186, v186, v250
	v_add_u32_e32 v187, v187, v250
	v_add_u32_e32 v188, v188, v250
	v_add_u32_e32 v189, v189, v250
	v_add_u32_e32 v190, v190, v250
	v_add_u32_e32 v191, v191, v250
	v_add_u32_e32 v192, v192, v250
	v_subrev_u32_e32 v252, s60, v170
	v_subrev_u32_e32 v255, s64, v172
	s_sub_u32 s1, s64, s60
	s_add_i32 s1, s1, 0xffffc000
	v_add_u32_e32 v254, 0x2000, v252
	v_add_u32_e32 v255, s1, v255
	v_add_u32_e32 v201, 0x2000, v255
	s_add_u32 s60, s60, 0xc000
	s_addc_u32 s61, s61, 0
	s_mov_b32 s42, 0x43dc0000
	s_mov_b64 s[54:55], -1
	v_mul_f32_e32 v71, 0x3db8aa3b, v168
	v_mov_b32_e32 v72, 0
	v_mov_b32_e32 v108, v164
	v_mov_b32_e32 v109, v165
	v_mov_b32_e32 v110, v166
	v_mov_b32_e32 v111, v167
	v_lshlrev_b32_e32 v164, 1, v193
	v_sub_u32_e32 v164, v164, v194
	v_add_u32_e32 v164, 0x400, v164
	s_cmp_eq_u32 s34, 0
	s_cbranch_scc1 .Lat_nsw
	v_swap_b32 v195, v196

.Lat_u0:
	ds_read_b128 v[112:115], v164
	v_mfma_i32_32x32x32_i8 v[84:99], v[242:245], v[140:143], v[84:99]
	ds_read_b128 v[116:119], v195 offset:6144
	ds_read_b128 v[120:123], v196 offset:6144
	s_cmp_gt_u32 s43, 29
	s_cbranch_scc1 .Lat_nok0
	s_add_i32 m0, s31, 49152
	ds_read_b128 v[124:127], v195 offset:4096
	global_load_lds_dwordx4 v252, s[60:61]
	s_add_i32 m0, s31, 57344
	v_mfma_i32_32x32x32_i8 v[84:99], v[246:249], v[144:147], v[84:99]
	global_load_lds_dwordx4 v254, s[60:61]

.Lat_v0:
	v_fma_f32 v86, v86, v250, v251
	v_fma_f32 v87, v87, v250, v251
	v_exp_f32_e32 v84, v84
	v_exp_f32_e32 v85, v85
	v_exp_f32_e32 v86, v86
	v_exp_f32_e32 v87, v87
	v_fma_f32 v88, v88, v250, v251
	v_fma_f32 v89, v89, v250, v251
	v_fma_f32 v90, v90, v250, v251
	v_fma_f32 v91, v91, v250, v251
	s_waitcnt lgkmcnt(8)
	v_mfma_f32_32x32x64_f8f6f4 v[18:33], v[108:115], v[124:131], v[18:33]
	v_add_f32_e32 v67, v84, v85
	v_add_f32_e32 v68, v86, v87
	v_exp_f32_e32 v88, v88
	v_exp_f32_e32 v89, v89
	v_exp_f32_e32 v90, v90
	v_exp_f32_e32 v91, v91
	v_add_f32_e32 v67, v67, v68
	v_cvt_pk_fp8_f32 v100, v84, v85
	v_cvt_pk_fp8_f32 v100, v86, v87 op_sel:[0,0,1]
	v_fma_f32 v92, v92, v250, v251
	v_fma_f32 v93, v93, v250, v251
	v_fma_f32 v94, v94, v250, v251
	v_fma_f32 v95, v95, v250, v251
	v_add_f32_e32 v68, v88, v89
	v_add_f32_e32 v69, v90, v91
	s_waitcnt lgkmcnt(6)
	v_mfma_f32_32x32x64_f8f6f4 v[50:65], v[108:115], v[202:209], v[50:65]
	ds_read_b128 v[202:205], v189 offset:32768
	ds_read_b128 v[206:209], v190 offset:32768
	v_exp_f32_e32 v92, v92
	v_exp_f32_e32 v93, v93
	v_exp_f32_e32 v94, v94
	v_exp_f32_e32 v95, v95
	v_add_f32_e32 v68, v68, v69
	v_cvt_pk_fp8_f32 v101, v88, v89
	v_cvt_pk_fp8_f32 v101, v90, v91 op_sel:[0,0,1]
	v_fma_f32 v96, v96, v250, v251
	v_fma_f32 v97, v97, v250, v251
	v_fma_f32 v98, v98, v250, v251
	v_fma_f32 v99, v99, v250, v251
	v_add_f32_e32 v67, v67, v68
	v_add_f32_e32 v68, v92, v93
	v_add_f32_e32 v69, v94, v95
	s_waitcnt lgkmcnt(6)
	v_mfma_f32_32x32x64_f8f6f4 v[34:49], v[108:115], v[210:217], v[34:49]
	ds_read_b128 v[210:213], v191 offset:32768
	ds_read_b128 v[214:217], v192 offset:32768
	v_exp_f32_e32 v96, v96
	v_exp_f32_e32 v97, v97
	v_exp_f32_e32 v98, v98
	v_exp_f32_e32 v99, v99
	v_add_f32_e32 v68, v68, v69
	v_cvt_pk_fp8_f32 v102, v92, v93
	v_cvt_pk_fp8_f32 v102, v94, v95 op_sel:[0,0,1]
	v_add_f32_e32 v67, v67, v68
	v_add_f32_e32 v68, v96, v97
	v_add_f32_e32 v69, v98, v99
	s_add_u32 s60, s60, 0x4000
	s_addc_u32 s61, s61, 0
	v_add_f32_e32 v68, v68, v69
	v_cvt_pk_fp8_f32 v103, v96, v97
	v_cvt_pk_fp8_f32 v103, v98, v99 op_sel:[0,0,1]
	v_add_f32_e32 v67, v67, v68
	ds_write_b128 v194, v[100:103] offset:8192
	v_max_f32_e32 v72, v72, v67
	v_add_f32_e32 v66, v66, v67
	s_add_i32 s43, s43, 1
	s_cmp_eq_u32 s43, 32
	s_cbranch_scc1 .Lat_last
	s_waitcnt lgkmcnt(7)
	v_mfma_i32_32x32x32_i8 v[84:99], v[218:221], v[132:135], v[226:241]
	v_mfma_i32_32x32x32_i8 v[84:99], v[222:225], v[136:139], v[84:99]
	s_waitcnt vmcnt(2) lgkmcnt(0)
	s_barrier
.Lat_u1:
	ds_read_b128 v[104:107], v164 offset:8192
	v_mfma_i32_32x32x32_i8 v[84:99], v[242:245], v[140:143], v[84:99]
	ds_read_b128 v[116:119], v195 offset:22528
	ds_read_b128 v[120:123], v196 offset:22528
	s_add_i32 m0, s31, 65536
	ds_read_b128 v[124:127], v195 offset:20480
	global_load_lds_dwordx4 v252, s[60:61]
	s_add_i32 m0, s31, 73728
	v_mfma_i32_32x32x32_i8 v[84:99], v[246:249], v[144:147], v[84:99]
	global_load_lds_dwordx4 v254, s[60:61]
	ds_read_b128 v[128:131], v196 offset:20480
	v_mfma_i32_32x32x32_i8 v[84:99], v[202:205], v[148:151], v[84:99]
	ds_read_b128 v[202:205], v195 offset:16384
	v_mfma_i32_32x32x32_i8 v[84:99], v[206:209], v[152:155], v[84:99]
	ds_read_b128 v[206:209], v196 offset:16384
	v_mfma_i32_32x32x32_i8 v[84:99], v[210:213], v[156:159], v[84:99]
	ds_read_b128 v[210:213], v195 offset:18432
	v_mfma_i32_32x32x32_i8 v[84:99], v[214:217], v[160:163], v[84:99]
	ds_read_b128 v[214:217], v196 offset:18432
	v_readlane_b32 s50, v182, s43
	s_waitcnt lgkmcnt(6)
	v_mfma_f32_32x32x64_f8f6f4 v[2:17], v[100:107], v[116:123], v[2:17]
	ds_read_b128 v[218:221], v185
	ds_read_b128 v[222:225], v186
	ds_read_b128 v[242:245], v187
	ds_read_b128 v[246:249], v188
	v_mul_f32_e32 v250, s50, v71
	v_fmamk_f32 v251, v250, 0xcb400000, v200
	s_mov_b32 m0, s31
	v_fma_f32 v84, v84, v250, v251
	global_load_lds_dwordx4 v255, s[60:61]
	s_add_i32 m0, s31, 8192
	v_fma_f32 v85, v85, v250, v251
	global_load_lds_dwordx4 v201, s[60:61]
	v_fma_f32 v86, v86, v250, v251
	v_fma_f32 v87, v87, v250, v251
	v_exp_f32_e32 v84, v84
	v_exp_f32_e32 v85, v85
	v_exp_f32_e32 v86, v86
	v_exp_f32_e32 v87, v87
	v_fma_f32 v88, v88, v250, v251
	v_fma_f32 v89, v89, v250, v251
	v_fma_f32 v90, v90, v250, v251
	v_fma_f32 v91, v91, v250, v251
	s_waitcnt lgkmcnt(8)
	v_mfma_f32_32x32x64_f8f6f4 v[18:33], v[100:107], v[124:131], v[18:33]
	v_add_f32_e32 v67, v84, v85
	v_add_f32_e32 v68, v86, v87
	v_exp_f32_e32 v88, v88
	v_exp_f32_e32 v89, v89
	v_exp_f32_e32 v90, v90
	v_exp_f32_e32 v91, v91
	v_add_f32_e32 v67, v67, v68
	v_cvt_pk_fp8_f32 v108, v84, v85
	v_cvt_pk_fp8_f32 v108, v86, v87 op_sel:[0,0,1]
	v_fma_f32 v92, v92, v250, v251
	v_fma_f32 v93, v93, v250, v251
	v_fma_f32 v94, v94, v250, v251
	v_fma_f32 v95, v95, v250, v251
	v_add_f32_e32 v68, v88, v89
	v_add_f32_e32 v69, v90, v91
	s_waitcnt lgkmcnt(6)
	v_mfma_f32_32x32x64_f8f6f4 v[50:65], v[100:107], v[202:209], v[50:65]
	ds_read_b128 v[202:205], v189
	ds_read_b128 v[206:209], v190
	v_exp_f32_e32 v92, v92
	v_exp_f32_e32 v93, v93
	v_exp_f32_e32 v94, v94
	v_exp_f32_e32 v95, v95
	v_add_f32_e32 v68, v68, v69
	v_cvt_pk_fp8_f32 v109, v88, v89
	v_cvt_pk_fp8_f32 v109, v90, v91 op_sel:[0,0,1]
	v_fma_f32 v96, v96, v250, v251
	v_fma_f32 v97, v97, v250, v251
	v_fma_f32 v98, v98, v250, v251
	v_fma_f32 v99, v99, v250, v251
	v_add_f32_e32 v67, v67, v68
	v_add_f32_e32 v68, v92, v93
	v_add_f32_e32 v69, v94, v95
	s_waitcnt lgkmcnt(6)
	v_mfma_f32_32x32x64_f8f6f4 v[34:49], v[100:107], v[210:217], v[34:49]
	ds_read_b128 v[210:213], v191
	ds_read_b128 v[214:217], v192
	v_exp_f32_e32 v96, v96
	v_exp_f32_e32 v97, v97
	v_exp_f32_e32 v98, v98
	v_exp_f32_e32 v99, v99
	v_add_f32_e32 v68, v68, v69
	v_cvt_pk_fp8_f32 v110, v92, v93
	v_cvt_pk_fp8_f32 v110, v94, v95 op_sel:[0,0,1]
	v_add_f32_e32 v67, v67, v68
	v_add_f32_e32 v68, v96, v97
	v_add_f32_e32 v69, v98, v99
	s_add_u32 s60, s60, 0x4000
	s_addc_u32 s61, s61, 0
	v_add_f32_e32 v68, v68, v69
	v_cvt_pk_fp8_f32 v111, v96, v97
	v_cvt_pk_fp8_f32 v111, v98, v99 op_sel:[0,0,1]
	v_add_f32_e32 v67, v67, v68
	ds_write_b128 v194, v[108:111]
	v_max_f32_e32 v72, v72, v67
	v_add_f32_e32 v66, v66, v67
	s_add_i32 s43, s43, 1
	s_waitcnt lgkmcnt(7)
	v_mfma_i32_32x32x32_i8 v[84:99], v[218:221], v[132:135], v[226:241]
	v_mfma_i32_32x32x32_i8 v[84:99], v[222:225], v[136:139], v[84:99]
	s_waitcnt vmcnt(2) lgkmcnt(0)
	s_barrier
.Lat_u2:
	ds_read_b128 v[112:115], v164
	v_mfma_i32_32x32x32_i8 v[84:99], v[242:245], v[140:143], v[84:99]
	ds_read_b128 v[116:119], v195 offset:38912
	ds_read_b128 v[120:123], v196 offset:38912
	s_add_i32 m0, s31, 81920
	ds_read_b128 v[124:127], v195 offset:36864
	global_load_lds_dwordx4 v252, s[60:61]
	s_add_i32 m0, s31, 90112
	v_mfma_i32_32x32x32_i8 v[84:99], v[246:249], v[144:147], v[84:99]
	global_load_lds_dwordx4 v254, s[60:61]
	ds_read_b128 v[128:131], v196 offset:36864
	v_mfma_i32_32x32x32_i8 v[84:99], v[202:205], v[148:151], v[84:99]
	ds_read_b128 v[202:205], v195 offset:32768
	v_mfma_i32_32x32x32_i8 v[84:99], v[206:209], v[152:155], v[84:99]
	ds_read_b128 v[206:209], v196 offset:32768
	v_mfma_i32_32x32x32_i8 v[84:99], v[210:213], v[156:159], v[84:99]
	ds_read_b128 v[210:213], v195 offset:34816
	v_mfma_i32_32x32x32_i8 v[84:99], v[214:217], v[160:163], v[84:99]
	ds_read_b128 v[214:217], v196 offset:34816
	v_readlane_b32 s50, v182, s43
	s_waitcnt lgkmcnt(6)
	v_mfma_f32_32x32x64_f8f6f4 v[2:17], v[108:115], v[116:123], v[2:17]
	ds_read_b128 v[218:221], v185 offset:16384
	ds_read_b128 v[222:225], v186 offset:16384
	ds_read_b128 v[242:245], v187 offset:16384
	ds_read_b128 v[246:249], v188 offset:16384
	v_mul_f32_e32 v250, s50, v71
	v_fmamk_f32 v251, v250, 0xcb400000, v200
	s_add_i32 m0, s31, 16384
	v_fma_f32 v84, v84, v250, v251
	global_load_lds_dwordx4 v255, s[60:61]
	s_add_i32 m0, s31, 24576
	v_fma_f32 v85, v85, v250, v251
	global_load_lds_dwordx4 v201, s[60:61]
	v_fma_f32 v86, v86, v250, v251
	v_fma_f32 v87, v87, v250, v251
	v_exp_f32_e32 v84, v84
	v_exp_f32_e32 v85, v85
	v_exp_f32_e32 v86, v86
	v_exp_f32_e32 v87, v87
	v_fma_f32 v88, v88, v250, v251
	v_fma_f32 v89, v89, v250, v251
	v_fma_f32 v90, v90, v250, v251
	v_fma_f32 v91, v91, v250, v251
	s_waitcnt lgkmcnt(8)
	v_mfma_f32_32x32x64_f8f6f4 v[18:33], v[108:115], v[124:131], v[18:33]
	v_add_f32_e32 v67, v84, v85
	v_add_f32_e32 v68, v86, v87
	v_exp_f32_e32 v88, v88
	v_exp_f32_e32 v89, v89
	v_exp_f32_e32 v90, v90
	v_exp_f32_e32 v91, v91
	v_add_f32_e32 v67, v67, v68
	v_cvt_pk_fp8_f32 v100, v84, v85
	v_cvt_pk_fp8_f32 v100, v86, v87 op_sel:[0,0,1]
	v_fma_f32 v92, v92, v250, v251
	v_fma_f32 v93, v93, v250, v251
	v_fma_f32 v94, v94, v250, v251
	v_fma_f32 v95, v95, v250, v251
	v_add_f32_e32 v68, v88, v89
	v_add_f32_e32 v69, v90, v91
	s_waitcnt lgkmcnt(6)
	v_mfma_f32_32x32x64_f8f6f4 v[50:65], v[108:115], v[202:209], v[50:65]
	ds_read_b128 v[202:205], v189 offset:16384
	ds_read_b128 v[206:209], v190 offset:16384
	v_exp_f32_e32 v92, v92
	v_exp_f32_e32 v93, v93
	v_exp_f32_e32 v94, v94
	v_exp_f32_e32 v95, v95
	v_add_f32_e32 v68, v68, v69
	v_cvt_pk_fp8_f32 v101, v88, v89
	v_cvt_pk_fp8_f32 v101, v90, v91 op_sel:[0,0,1]
	v_fma_f32 v96, v96, v250, v251
	v_fma_f32 v97, v97, v250, v251
	v_fma_f32 v98, v98, v250, v251
	v_fma_f32 v99, v99, v250, v251
	v_add_f32_e32 v67, v67, v68
	v_add_f32_e32 v68, v92, v93
	v_add_f32_e32 v69, v94, v95
	s_waitcnt lgkmcnt(6)
	v_mfma_f32_32x32x64_f8f6f4 v[34:49], v[108:115], v[210:217], v[34:49]
	ds_read_b128 v[210:213], v191 offset:16384
	ds_read_b128 v[214:217], v192 offset:16384
	v_exp_f32_e32 v96, v96
	v_exp_f32_e32 v97, v97
	v_exp_f32_e32 v98, v98
	v_exp_f32_e32 v99, v99
	v_add_f32_e32 v68, v68, v69
	v_cvt_pk_fp8_f32 v102, v92, v93
	v_cvt_pk_fp8_f32 v102, v94, v95 op_sel:[0,0,1]
	v_add_f32_e32 v67, v67, v68
	v_add_f32_e32 v68, v96, v97
	v_add_f32_e32 v69, v98, v99
	s_add_u32 s60, s60, 0x4000
	s_addc_u32 s61, s61, 0
	v_add_f32_e32 v68, v68, v69
	v_cvt_pk_fp8_f32 v103, v96, v97
	v_cvt_pk_fp8_f32 v103, v98, v99 op_sel:[0,0,1]
	v_add_f32_e32 v67, v67, v68
	ds_write_b128 v194, v[100:103] offset:8192
	v_max_f32_e32 v72, v72, v67
	v_add_f32_e32 v66, v66, v67
	s_add_i32 s43, s43, 1
	s_waitcnt lgkmcnt(7)
	v_mfma_i32_32x32x32_i8 v[84:99], v[218:221], v[132:135], v[226:241]
	v_mfma_i32_32x32x32_i8 v[84:99], v[222:225], v[136:139], v[84:99]
	s_waitcnt vmcnt(2) lgkmcnt(0)
	s_barrier
.Lat_u3:
	ds_read_b128 v[104:107], v164 offset:8192
	v_mfma_i32_32x32x32_i8 v[84:99], v[242:245], v[140:143], v[84:99]
	ds_read_b128 v[116:119], v195 offset:6144
	ds_read_b128 v[120:123], v196 offset:6144
	s_add_i32 m0, s31, 49152
	ds_read_b128 v[124:127], v195 offset:4096
	global_load_lds_dwordx4 v252, s[60:61]
	s_add_i32 m0, s31, 57344
	v_mfma_i32_32x32x32_i8 v[84:99], v[246:249], v[144:147], v[84:99]
	global_load_lds_dwordx4 v254, s[60:61]
	ds_read_b128 v[128:131], v196 offset:4096
	v_mfma_i32_32x32x32_i8 v[84:99], v[202:205], v[148:151], v[84:99]
	ds_read_b128 v[202:205], v195
	v_mfma_i32_32x32x32_i8 v[84:99], v[206:209], v[152:155], v[84:99]
	ds_read_b128 v[206:209], v196
	v_mfma_i32_32x32x32_i8 v[84:99], v[210:213], v[156:159], v[84:99]
	ds_read_b128 v[210:213], v195 offset:2048
	v_mfma_i32_32x32x32_i8 v[84:99], v[214:217], v[160:163], v[84:99]
	ds_read_b128 v[214:217], v196 offset:2048
	v_readlane_b32 s50, v182, s43
	s_waitcnt lgkmcnt(6)
	v_mfma_f32_32x32x64_f8f6f4 v[2:17], v[100:107], v[116:123], v[2:17]
	ds_read_b128 v[218:221], v185 offset:32768
	ds_read_b128 v[222:225], v186 offset:32768
	ds_read_b128 v[242:245], v187 offset:32768
	ds_read_b128 v[246:249], v188 offset:32768
	v_mul_f32_e32 v250, s50, v71
	v_fmamk_f32 v251, v250, 0xcb400000, v200
	s_add_i32 m0, s31, 32768
	v_fma_f32 v84, v84, v250, v251
	global_load_lds_dwordx4 v255, s[60:61]
	s_add_i32 m0, s31, 40960
	v_fma_f32 v85, v85, v250, v251
	global_load_lds_dwordx4 v201, s[60:61]
	v_fma_f32 v86, v86, v250, v251
	v_fma_f32 v87, v87, v250, v251
	v_exp_f32_e32 v84, v84
	v_exp_f32_e32 v85, v85
	v_exp_f32_e32 v86, v86
	v_exp_f32_e32 v87, v87
	v_fma_f32 v88, v88, v250, v251
	v_fma_f32 v89, v89, v250, v251
	v_fma_f32 v90, v90, v250, v251
	v_fma_f32 v91, v91, v250, v251
	s_waitcnt lgkmcnt(8)
	v_mfma_f32_32x32x64_f8f6f4 v[18:33], v[100:107], v[124:131], v[18:33]
	v_add_f32_e32 v67, v84, v85
	v_add_f32_e32 v68, v86, v87
	v_exp_f32_e32 v88, v88
	v_exp_f32_e32 v89, v89
	v_exp_f32_e32 v90, v90
	v_exp_f32_e32 v91, v91
	v_add_f32_e32 v67, v67, v68
	v_cvt_pk_fp8_f32 v108, v84, v85
	v_cvt_pk_fp8_f32 v108, v86, v87 op_sel:[0,0,1]
	v_fma_f32 v92, v92, v250, v251
	v_fma_f32 v93, v93, v250, v251
	v_fma_f32 v94, v94, v250, v251
	v_fma_f32 v95, v95, v250, v251
	v_add_f32_e32 v68, v88, v89
	v_add_f32_e32 v69, v90, v91
	s_waitcnt lgkmcnt(6)
	v_mfma_f32_32x32x64_f8f6f4 v[50:65], v[100:107], v[202:209], v[50:65]
	ds_read_b128 v[202:205], v189 offset:32768
	ds_read_b128 v[206:209], v190 offset:32768
	v_exp_f32_e32 v92, v92
	v_exp_f32_e32 v93, v93
	v_exp_f32_e32 v94, v94
	v_exp_f32_e32 v95, v95
	v_add_f32_e32 v68, v68, v69
	v_cvt_pk_fp8_f32 v109, v88, v89
	v_cvt_pk_fp8_f32 v109, v90, v91 op_sel:[0,0,1]
	v_fma_f32 v96, v96, v250, v251
	v_fma_f32 v97, v97, v250, v251
	v_fma_f32 v98, v98, v250, v251
	v_fma_f32 v99, v99, v250, v251
	v_add_f32_e32 v67, v67, v68
	v_add_f32_e32 v68, v92, v93
	v_add_f32_e32 v69, v94, v95
	s_waitcnt lgkmcnt(6)
	v_mfma_f32_32x32x64_f8f6f4 v[34:49], v[100:107], v[210:217], v[34:49]
	ds_read_b128 v[210:213], v191 offset:32768
	ds_read_b128 v[214:217], v192 offset:32768
	v_exp_f32_e32 v96, v96
	v_exp_f32_e32 v97, v97
	v_exp_f32_e32 v98, v98
	v_exp_f32_e32 v99, v99
	v_add_f32_e32 v68, v68, v69
	v_cvt_pk_fp8_f32 v110, v92, v93
	v_cvt_pk_fp8_f32 v110, v94, v95 op_sel:[0,0,1]
	v_add_f32_e32 v67, v67, v68
	v_add_f32_e32 v68, v96, v97
	v_add_f32_e32 v69, v98, v99
	s_add_u32 s60, s60, 0x4000
	s_addc_u32 s61, s61, 0
	v_add_f32_e32 v68, v68, v69
	v_cvt_pk_fp8_f32 v111, v96, v97
	v_cvt_pk_fp8_f32 v111, v98, v99 op_sel:[0,0,1]
	v_add_f32_e32 v67, v67, v68
	ds_write_b128 v194, v[108:111]
	v_max_f32_e32 v72, v72, v67
	v_add_f32_e32 v66, v66, v67
	s_add_i32 s43, s43, 1
	s_waitcnt lgkmcnt(7)
	v_mfma_i32_32x32x32_i8 v[84:99], v[218:221], v[132:135], v[226:241]
	v_mfma_i32_32x32x32_i8 v[84:99], v[222:225], v[136:139], v[84:99]
	s_waitcnt vmcnt(2) lgkmcnt(0)
	s_barrier
.Lat_u4:
	ds_read_b128 v[112:115], v164
	v_mfma_i32_32x32x32_i8 v[84:99], v[242:245], v[140:143], v[84:99]
	ds_read_b128 v[116:119], v195 offset:22528
	ds_read_b128 v[120:123], v196 offset:22528
	s_add_i32 m0, s31, 65536
	ds_read_b128 v[124:127], v195 offset:20480
	global_load_lds_dwordx4 v252, s[60:61]
	s_add_i32 m0, s31, 73728
	v_mfma_i32_32x32x32_i8 v[84:99], v[246:249], v[144:147], v[84:99]
	global_load_lds_dwordx4 v254, s[60:61]
	ds_read_b128 v[128:131], v196 offset:20480
	v_mfma_i32_32x32x32_i8 v[84:99], v[202:205], v[148:151], v[84:99]
	ds_read_b128 v[202:205], v195 offset:16384
	v_mfma_i32_32x32x32_i8 v[84:99], v[206:209], v[152:155], v[84:99]
	ds_read_b128 v[206:209], v196 offset:16384
	v_mfma_i32_32x32x32_i8 v[84:99], v[210:213], v[156:159], v[84:99]
	ds_read_b128 v[210:213], v195 offset:18432
	v_mfma_i32_32x32x32_i8 v[84:99], v[214:217], v[160:163], v[84:99]
	ds_read_b128 v[214:217], v196 offset:18432
	v_readlane_b32 s50, v182, s43
	s_waitcnt lgkmcnt(6)
	v_mfma_f32_32x32x64_f8f6f4 v[2:17], v[108:115], v[116:123], v[2:17]
	ds_read_b128 v[218:221], v185
	ds_read_b128 v[222:225], v186
	ds_read_b128 v[242:245], v187
	ds_read_b128 v[246:249], v188
	v_mul_f32_e32 v250, s50, v71
	v_fmamk_f32 v251, v250, 0xcb400000, v200
	s_mov_b32 m0, s31
	v_fma_f32 v84, v84, v250, v251
	global_load_lds_dwordx4 v255, s[60:61]
	s_add_i32 m0, s31, 8192
	v_fma_f32 v85, v85, v250, v251
	global_load_lds_dwordx4 v201, s[60:61]
	v_fma_f32 v86, v86, v250, v251
	v_fma_f32 v87, v87, v250, v251
	v_exp_f32_e32 v84, v84
	v_exp_f32_e32 v85, v85
	v_exp_f32_e32 v86, v86
	v_exp_f32_e32 v87, v87
	v_fma_f32 v88, v88, v250, v251
	v_fma_f32 v89, v89, v250, v251
	v_fma_f32 v90, v90, v250, v251
	v_fma_f32 v91, v91, v250, v251
	s_waitcnt lgkmcnt(8)
	v_mfma_f32_32x32x64_f8f6f4 v[18:33], v[108:115], v[124:131], v[18:33]
	v_add_f32_e32 v67, v84, v85
	v_add_f32_e32 v68, v86, v87
	v_exp_f32_e32 v88, v88
	v_exp_f32_e32 v89, v89
	v_exp_f32_e32 v90, v90
	v_exp_f32_e32 v91, v91
	v_add_f32_e32 v67, v67, v68
	v_cvt_pk_fp8_f32 v100, v84, v85
	v_cvt_pk_fp8_f32 v100, v86, v87 op_sel:[0,0,1]
	v_fma_f32 v92, v92, v250, v251
	v_fma_f32 v93, v93, v250, v251
	v_fma_f32 v94, v94, v250, v251
	v_fma_f32 v95, v95, v250, v251
	v_add_f32_e32 v68, v88, v89
	v_add_f32_e32 v69, v90, v91
	s_waitcnt lgkmcnt(6)
	v_mfma_f32_32x32x64_f8f6f4 v[50:65], v[108:115], v[202:209], v[50:65]
	ds_read_b128 v[202:205], v189
	ds_read_b128 v[206:209], v190
	v_exp_f32_e32 v92, v92
	v_exp_f32_e32 v93, v93
	v_exp_f32_e32 v94, v94
	v_exp_f32_e32 v95, v95
	v_add_f32_e32 v68, v68, v69
	v_cvt_pk_fp8_f32 v101, v88, v89
	v_cvt_pk_fp8_f32 v101, v90, v91 op_sel:[0,0,1]
	v_fma_f32 v96, v96, v250, v251
	v_fma_f32 v97, v97, v250, v251
	v_fma_f32 v98, v98, v250, v251
	v_fma_f32 v99, v99, v250, v251
	v_add_f32_e32 v67, v67, v68
	v_add_f32_e32 v68, v92, v93
	v_add_f32_e32 v69, v94, v95
	s_waitcnt lgkmcnt(6)
	v_mfma_f32_32x32x64_f8f6f4 v[34:49], v[108:115], v[210:217], v[34:49]
	ds_read_b128 v[210:213], v191
	ds_read_b128 v[214:217], v192
	v_exp_f32_e32 v96, v96
	v_exp_f32_e32 v97, v97
	v_exp_f32_e32 v98, v98
	v_exp_f32_e32 v99, v99
	v_add_f32_e32 v68, v68, v69
	v_cvt_pk_fp8_f32 v102, v92, v93
	v_cvt_pk_fp8_f32 v102, v94, v95 op_sel:[0,0,1]
	v_add_f32_e32 v67, v67, v68
	v_add_f32_e32 v68, v96, v97
	v_add_f32_e32 v69, v98, v99
	s_add_u32 s60, s60, 0x4000
	s_addc_u32 s61, s61, 0
	v_add_f32_e32 v68, v68, v69
	v_cvt_pk_fp8_f32 v103, v96, v97
	v_cvt_pk_fp8_f32 v103, v98, v99 op_sel:[0,0,1]
	v_add_f32_e32 v67, v67, v68
	ds_write_b128 v194, v[100:103] offset:8192
	v_max_f32_e32 v72, v72, v67
	v_add_f32_e32 v66, v66, v67
	s_add_i32 s43, s43, 1
	s_waitcnt lgkmcnt(7)
	v_mfma_i32_32x32x32_i8 v[84:99], v[218:221], v[132:135], v[226:241]
	v_mfma_i32_32x32x32_i8 v[84:99], v[222:225], v[136:139], v[84:99]
	s_waitcnt vmcnt(2) lgkmcnt(0)
	s_barrier
.Lat_u5:
	ds_read_b128 v[104:107], v164 offset:8192
	v_mfma_i32_32x32x32_i8 v[84:99], v[242:245], v[140:143], v[84:99]
	ds_read_b128 v[116:119], v195 offset:38912
	ds_read_b128 v[120:123], v196 offset:38912
	s_cmp_gt_u32 s43, 29
	s_cbranch_scc1 .Lat_nok5
	s_add_i32 m0, s31, 81920
	ds_read_b128 v[124:127], v195 offset:36864
	global_load_lds_dwordx4 v252, s[60:61]
	s_add_i32 m0, s31, 90112
	v_mfma_i32_32x32x32_i8 v[84:99], v[246:249], v[144:147], v[84:99]
	global_load_lds_dwordx4 v254, s[60:61]
.Lat_k5:
	ds_read_b128 v[128:131], v196 offset:36864
	v_mfma_i32_32x32x32_i8 v[84:99], v[202:205], v[148:151], v[84:99]
	ds_read_b128 v[202:205], v195 offset:32768
	v_mfma_i32_32x32x32_i8 v[84:99], v[206:209], v[152:155], v[84:99]
	ds_read_b128 v[206:209], v196 offset:32768
	v_mfma_i32_32x32x32_i8 v[84:99], v[210:213], v[156:159], v[84:99]
	ds_read_b128 v[210:213], v195 offset:34816
	v_mfma_i32_32x32x32_i8 v[84:99], v[214:217], v[160:163], v[84:99]
	ds_read_b128 v[214:217], v196 offset:34816
	v_readlane_b32 s50, v182, s43
	s_waitcnt lgkmcnt(6)
	v_mfma_f32_32x32x64_f8f6f4 v[2:17], v[100:107], v[116:123], v[2:17]
	ds_read_b128 v[218:221], v185 offset:16384
	ds_read_b128 v[222:225], v186 offset:16384
	ds_read_b128 v[242:245], v187 offset:16384
	ds_read_b128 v[246:249], v188 offset:16384
	v_mul_f32_e32 v250, s50, v71
	v_fmamk_f32 v251, v250, 0xcb400000, v200
	s_add_i32 m0, s31, 16384
	v_fma_f32 v84, v84, v250, v251
	global_load_lds_dwordx4 v255, s[60:61]
	s_add_i32 m0, s31, 24576
	v_fma_f32 v85, v85, v250, v251
	global_load_lds_dwordx4 v201, s[60:61]
	v_fma_f32 v86, v86, v250, v251
	v_fma_f32 v87, v87, v250, v251
	v_exp_f32_e32 v84, v84
	v_exp_f32_e32 v85, v85
	v_exp_f32_e32 v86, v86
	v_exp_f32_e32 v87, v87
	v_fma_f32 v88, v88, v250, v251
	v_fma_f32 v89, v89, v250, v251
	v_fma_f32 v90, v90, v250, v251
	v_fma_f32 v91, v91, v250, v251
	s_waitcnt lgkmcnt(8)
	v_mfma_f32_32x32x64_f8f6f4 v[18:33], v[100:107], v[124:131], v[18:33]
	v_add_f32_e32 v67, v84, v85
	v_add_f32_e32 v68, v86, v87
	v_exp_f32_e32 v88, v88
	v_exp_f32_e32 v89, v89
	v_exp_f32_e32 v90, v90
	v_exp_f32_e32 v91, v91
	v_add_f32_e32 v67, v67, v68
	v_cvt_pk_fp8_f32 v108, v84, v85
	v_cvt_pk_fp8_f32 v108, v86, v87 op_sel:[0,0,1]
	v_fma_f32 v92, v92, v250, v251
	v_fma_f32 v93, v93, v250, v251
	v_fma_f32 v94, v94, v250, v251
	v_fma_f32 v95, v95, v250, v251
	v_add_f32_e32 v68, v88, v89
	v_add_f32_e32 v69, v90, v91
	s_waitcnt lgkmcnt(6)
	v_mfma_f32_32x32x64_f8f6f4 v[50:65], v[100:107], v[202:209], v[50:65]
	ds_read_b128 v[202:205], v189 offset:16384
	ds_read_b128 v[206:209], v190 offset:16384
	v_exp_f32_e32 v92, v92
	v_exp_f32_e32 v93, v93
	v_exp_f32_e32 v94, v94
	v_exp_f32_e32 v95, v95
	v_add_f32_e32 v68, v68, v69
	v_cvt_pk_fp8_f32 v109, v88, v89
	v_cvt_pk_fp8_f32 v109, v90, v91 op_sel:[0,0,1]
	v_fma_f32 v96, v96, v250, v251
	v_fma_f32 v97, v97, v250, v251
	v_fma_f32 v98, v98, v250, v251
	v_fma_f32 v99, v99, v250, v251
	v_add_f32_e32 v67, v67, v68
	v_add_f32_e32 v68, v92, v93
	v_add_f32_e32 v69, v94, v95
	s_waitcnt lgkmcnt(6)
	v_mfma_f32_32x32x64_f8f6f4 v[34:49], v[100:107], v[210:217], v[34:49]
	ds_read_b128 v[210:213], v191 offset:16384
	ds_read_b128 v[214:217], v192 offset:16384
	v_exp_f32_e32 v96, v96
	v_exp_f32_e32 v97, v97
	v_exp_f32_e32 v98, v98
	v_exp_f32_e32 v99, v99
	v_add_f32_e32 v68, v68, v69
	v_cvt_pk_fp8_f32 v110, v92, v93
	v_cvt_pk_fp8_f32 v110, v94, v95 op_sel:[0,0,1]
	v_add_f32_e32 v67, v67, v68
	v_add_f32_e32 v68, v96, v97
	v_add_f32_e32 v69, v98, v99
	s_add_u32 s60, s60, 0x4000
	s_addc_u32 s61, s61, 0
	v_add_f32_e32 v68, v68, v69
	v_cvt_pk_fp8_f32 v111, v96, v97
	v_cvt_pk_fp8_f32 v111, v98, v99 op_sel:[0,0,1]
	v_add_f32_e32 v67, v67, v68
	ds_write_b128 v194, v[108:111]
	v_max_f32_e32 v72, v72, v67
	v_add_f32_e32 v66, v66, v67
	s_add_i32 s43, s43, 1
	s_waitcnt lgkmcnt(7)
	v_mfma_i32_32x32x32_i8 v[84:99], v[218:221], v[132:135], v[226:241]
	v_mfma_i32_32x32x32_i8 v[84:99], v[222:225], v[136:139], v[84:99]
	s_cmp_gt_u32 s43, 30
	s_cbranch_scc1 .Lat_drain
	s_waitcnt vmcnt(2) lgkmcnt(0)
	s_barrier
	s_branch .Lat_u0

.Lat_nsw2:
	v_cmp_ge_f32_e64 s[54:55], s42, v72
	s_nop 3
	s_cmp_lg_u64 s[54:55], exec
	s_cselect_b32 s1, 1, 0
	s_or_b32 s39, s39, s1
	v_add_u32_e32 v250, 0xc000, v184
	v_sub_u32_e32 v185, v185, v250
	v_sub_u32_e32 v186, v186, v250
	v_sub_u32_e32 v187, v187, v250
	v_sub_u32_e32 v188, v188, v250
	v_sub_u32_e32 v189, v189, v250
	v_sub_u32_e32 v190, v190, v250
	v_sub_u32_e32 v191, v191, v250
	v_sub_u32_e32 v192, v192, v250
